# attention queue: next unit ticket taken in the second-to-last key-loop trip (hides the dequeue round trip), on top of v046
# speedup vs baseline: 1.0174x; 1.0030x over previous
.LBB0_949:
	s_or_b64 exec, exec, s[0:1]
	s_lshl_b32 s64, s59, 6
	s_lshl_b64 s[0:1], s[64:65], 2
	v_lshl_add_u32 v17, s14, 6, v118
	s_add_u32 s10, s72, s0
	s_mov_b32 s0, 0x2aaaaaab
	v_mul_hi_i32 v1, v17, s0
	v_lshrrev_b32_e32 v2, 31, v1
	v_ashrrev_i32_e32 v1, 1, v1
	v_add_u32_e32 v164, v1, v2
	v_mul_lo_u32 v1, v164, 12
	v_add_u32_e32 v0, 0x200, v17
	v_sub_u32_e32 v1, v17, v1
	v_lshlrev_b32_e32 v166, 3, v1
	v_mul_hi_i32 v1, v0, s0
	ds_swizzle_b32 v2, v5 offset:swizzle(SWAP,1)
	v_lshrrev_b32_e32 v3, 31, v1
	v_ashrrev_i32_e32 v1, 1, v1
	v_add_u32_e32 v168, v1, v3
	v_mul_lo_u32 v3, v168, 12
	v_sub_u32_e32 v0, v0, v3
	v_max_f32_e32 v1, v5, v5
	s_waitcnt lgkmcnt(0)
	v_max_f32_e32 v2, v2, v2
	v_lshlrev_b32_e32 v170, 3, v0
	ds_swizzle_b32 v0, v4 offset:swizzle(SWAP,1)
	v_max_f32_e32 v1, v1, v2
	ds_swizzle_b32 v2, v1 offset:swizzle(SWAP,2)
	v_max_f32_e32 v3, v4, v4
	s_addc_u32 s11, s73, s1
	s_waitcnt lgkmcnt(0)
	v_max_f32_e32 v0, v0, v0
	v_max_f32_e32 v0, v3, v0
	v_max_f32_e32 v2, v2, v2
	ds_swizzle_b32 v3, v0 offset:swizzle(SWAP,2)
	v_max_f32_e32 v1, v1, v2
	ds_swizzle_b32 v2, v1 offset:swizzle(SWAP,4)
	v_mad_i64_i32 v[174:175], s[2:3], v164, s88, 0
	s_waitcnt lgkmcnt(0)
	v_max_f32_e32 v3, v3, v3
	v_max_f32_e32 v0, v0, v3
	v_max_f32_e32 v2, v2, v2
	ds_swizzle_b32 v3, v0 offset:swizzle(SWAP,4)
	v_max_f32_e32 v1, v1, v2
	ds_swizzle_b32 v2, v1 offset:swizzle(SWAP,8)
	s_add_u32 s12, s8, 0x25c00000
	v_ashrrev_i32_e32 v16, 3, v17
	s_waitcnt lgkmcnt(0)
	v_max_f32_e32 v3, v3, v3
	v_max_f32_e32 v0, v0, v3
	v_max_f32_e32 v2, v2, v2
	ds_swizzle_b32 v3, v0 offset:swizzle(SWAP,8)
	v_max_f32_e32 v1, v1, v2
	ds_swizzle_b32 v2, v1 offset:swizzle(SWAP,16)
	v_lshlrev_b32_e32 v4, 3, v118
	s_mov_b32 s0, 0x3f828f5c
	s_waitcnt lgkmcnt(0)
	v_max_f32_e32 v3, v3, v3
	v_max_f32_e32 v0, v0, v3
	v_max_f32_e32 v2, v2, v2
	ds_swizzle_b32 v3, v0 offset:swizzle(SWAP,16)
	v_max_f32_e32 v1, v1, v2
	v_mov_b32_e32 v2, v1
	s_nop 1
	v_permlane32_swap_b32_e32 v1, v2
	v_max_f32_e32 v2, v2, v2
	v_max_f32_e32 v1, v1, v1
	v_max_f32_e32 v1, v1, v2
	s_waitcnt lgkmcnt(0)
	v_max_f32_e32 v2, v3, v3
	v_max_f32_e32 v0, v0, v2
	v_mov_b32_e32 v2, v0
	s_nop 1
	v_permlane32_swap_b32_e32 v0, v2
	v_max_f32_e32 v2, v2, v2
	v_max_f32_e32 v0, v0, v0
	v_max_f32_e32 v0, v0, v2
	v_mul_f32_e32 v1, 0x41622ae0, v1
	v_mul_f32_e32 v0, v1, v0
	s_movk_i32 s2, 0x100
	s_movk_i32 s4, 0xff
	s_addc_u32 s13, s9, 0
	v_and_b32_e32 v18, 56, v4
	v_fma_f32 v0, v0, s0, 0.5
	v_cmp_eq_u32_e64 s[0:1], 0, v17
	v_cmp_gt_i32_e64 s[2:3], s2, v17
	v_cmp_lt_i32_e64 s[4:5], s4, v17
	v_ashrrev_i32_e32 v17, 31, v16
	s_add_u32 s20, s8, 0x2ac00000
	v_lshlrev_b32_e32 v172, 1, v18
	v_and_b32_e32 v236, 0x30, v18
	v_lshlrev_b32_e32 v236, 1, v236
	v_and_b32_e32 v237, 8, v18
	v_or_b32_e32 v236, v236, v237
	v_lshlrev_b64 v[18:19], 13, v[16:17]
	v_add_u32_e32 v17, 64, v168
	s_addc_u32 s21, s9, 0
	s_lshl_b32 s22, s14, 5
	v_mad_i64_i32 v[176:177], s[14:15], v168, s88, 0
	v_mad_i64_i32 v[178:179], s[14:15], v17, s88, 0
	v_and_b32_e32 v208, 0x60, v118
	v_lshl_add_u64 v[22:23], s[8:9], 0, v[208:209]
	s_mov_b64 s[14:15], 0x200000
	v_lshl_add_u64 v[182:183], v[22:23], 0, s[14:15]
	s_mov_b64 s[14:15], 0x300000
	v_lshl_add_u64 v[184:185], v[22:23], 0, s[14:15]
	s_movk_i32 s14, 0x68
	v_mul_lo_u32 v17, v164, s14
	s_waitcnt vmcnt(0)
	v_add_lshl_u32 v161, v17, v166, 1
	v_mul_lo_u32 v17, v168, s14
	s_movk_i32 s14, 0x48
	v_mul_lo_u32 v189, v16, s14
	v_lshlrev_b32_e32 v16, 1, v189
	v_add3_u32 v220, 0, v236, v16
	v_add_u32_e32 v16, 0x80, v168
	v_lshl_add_u64 v[20:21], s[8:9], 0, v[18:19]
	v_mad_i64_i32 v[186:187], s[14:15], v16, s88, 0
	v_mov_b32_e32 v173, v209
	v_add_lshl_u32 v181, v17, v170, 1
	v_lshl_add_u64 v[16:17], v[20:21], 0, v[172:173]
	s_mov_b64 s[14:15], 0x2c400000
	v_lshl_add_u64 v[190:191], v[16:17], 0, s[14:15]
	v_and_b32_e32 v16, 7, v118
	v_lshl_or_b32 v18, v16, 4, v18
	v_ashrrev_i32_e32 v171, 31, v170
	v_lshl_add_u64 v[16:17], s[8:9], 0, v[18:19]
	s_mov_b64 s[14:15], 0x2c400180
	v_lshl_add_u64 v[192:193], v[16:17], 0, s[14:15]
	s_add_u32 s14, s8, 0x2ac09000
	v_lshlrev_b64 v[16:17], 1, v[170:171]
	v_ashrrev_i32_e32 v167, 31, v166
	s_addc_u32 s15, s9, 0
	v_mad_i64_i32 v[16:17], s[16:17], v168, s88, v[16:17]
	v_lshl_add_u64 v[194:195], s[14:15], 0, v[16:17]
	v_lshlrev_b64 v[16:17], 1, v[166:167]
	v_lshrrev_b32_e32 v24, 5, v118
	v_xor_b32_e32 v0, 0x80000000, v0
	v_mad_i64_i32 v[16:17], s[16:17], v164, s88, v[16:17]
	v_mov_b32_e32 v1, v0
	v_mov_b32_e32 v2, v0
	v_mov_b32_e32 v3, v0
	v_mov_b32_e32 v4, v0
	v_mov_b32_e32 v5, v0
	v_mov_b32_e32 v6, v0
	v_mov_b32_e32 v7, v0
	v_mov_b32_e32 v8, v0
	v_mov_b32_e32 v9, v0
	v_mov_b32_e32 v10, v0
	v_mov_b32_e32 v11, v0
	v_mov_b32_e32 v12, v0
	v_mov_b32_e32 v13, v0
	v_mov_b32_e32 v14, v0
	v_mov_b32_e32 v15, v0
	v_ashrrev_i32_e32 v165, 31, v164
	v_ashrrev_i32_e32 v169, 31, v168
	v_lshlrev_b32_e32 v180, 3, v24
	v_mov_b32_e32 v163, v209
	v_mul_u32_u24_e32 v221, 0xd0, v160
	v_mul_u32_u24_e32 v222, 0x90, v160
	v_lshlrev_b32_e32 v188, 2, v24
	v_lshl_add_u64 v[196:197], s[14:15], 0, v[16:17]
	s_mov_b32 s39, 0
	s_branch .LBB0_952
.LBB0_950:
	s_waitcnt vmcnt(0)
	v_readfirstlane_b32 s38, v241
	v_mov_b32_e32 v48, v173
	s_nop 1
	v_permlane32_swap_b32_e32 v173, v48
	v_add_f32_e32 v48, v173, v48
	v_div_scale_f32 v49, s[14:15], v48, v48, 1.0
	v_rcp_f32_e32 v50, v49
	s_lshl_b32 s64, s23, 7
	v_lshlrev_b32_e32 v208, 1, v188
	s_mov_b64 s[14:15], 0x23c00200
	v_fma_f32 v51, -v49, v50, 1.0
	v_fmac_f32_e32 v50, v51, v50
	v_div_scale_f32 v51, vcc, 1.0, v48, 1.0
	v_mul_f32_e32 v52, v51, v50
	v_fma_f32 v53, -v49, v52, v51
	v_fmac_f32_e32 v52, v53, v50
	v_fma_f32 v49, -v49, v52, v51
	v_div_fmas_f32 v49, v49, v50, v52
	v_lshlrev_b64 v[50:51], 11, v[200:201]
	v_lshl_add_u64 v[50:51], s[8:9], 0, v[50:51]
	v_lshl_add_u64 v[50:51], v[50:51], 0, s[64:65]
	v_div_fixup_f32 v48, v49, v48, 1.0
	v_lshl_add_u64 v[50:51], v[50:51], 0, v[208:209]
	v_lshl_add_u64 v[52:53], v[50:51], 0, s[14:15]
	v_pk_mul_f32 v[32:33], v[32:33], v[48:49] op_sel_hi:[1,0]
	v_pk_mul_f32 v[34:35], v[34:35], v[48:49] op_sel_hi:[1,0]
	s_mov_b32 s14, 0x23c00000
	v_cvt_pk_bf16_f32 v32, v32, v33
	v_cvt_pk_bf16_f32 v33, v34, v35
	v_add_co_u32_e32 v34, vcc, s14, v50
	v_pk_mul_f32 v[16:17], v[16:17], v[48:49] op_sel_hi:[1,0]
	v_pk_mul_f32 v[18:19], v[18:19], v[48:49] op_sel_hi:[1,0]
	v_addc_co_u32_e32 v35, vcc, 0, v51, vcc
	v_cvt_pk_bf16_f32 v16, v16, v17
	v_cvt_pk_bf16_f32 v17, v18, v19
	global_store_dwordx2 v[34:35], v[32:33], off offset:512
	v_pk_mul_f32 v[32:33], v[36:37], v[48:49] op_sel_hi:[1,0]
	v_pk_mul_f32 v[34:35], v[38:39], v[48:49] op_sel_hi:[1,0]
	global_store_dwordx2 v[52:53], v[16:17], off offset:64
	v_pk_mul_f32 v[16:17], v[20:21], v[48:49] op_sel_hi:[1,0]
	v_pk_mul_f32 v[18:19], v[22:23], v[48:49] op_sel_hi:[1,0]
	v_cvt_pk_bf16_f32 v32, v32, v33
	v_cvt_pk_bf16_f32 v33, v34, v35
	v_cvt_pk_bf16_f32 v16, v16, v17
	v_cvt_pk_bf16_f32 v17, v18, v19
	global_store_dwordx2 v[52:53], v[32:33], off offset:16
	v_pk_mul_f32 v[32:33], v[40:41], v[48:49] op_sel_hi:[1,0]
	v_pk_mul_f32 v[34:35], v[42:43], v[48:49] op_sel_hi:[1,0]
	global_store_dwordx2 v[52:53], v[16:17], off offset:80
	v_pk_mul_f32 v[16:17], v[24:25], v[48:49] op_sel_hi:[1,0]
	v_pk_mul_f32 v[18:19], v[26:27], v[48:49] op_sel_hi:[1,0]
	v_cvt_pk_bf16_f32 v32, v32, v33
	v_cvt_pk_bf16_f32 v33, v34, v35
	v_cvt_pk_bf16_f32 v16, v16, v17
	v_cvt_pk_bf16_f32 v17, v18, v19
	global_store_dwordx2 v[52:53], v[32:33], off offset:32
	v_pk_mul_f32 v[32:33], v[44:45], v[48:49] op_sel_hi:[1,0]
	v_pk_mul_f32 v[34:35], v[46:47], v[48:49] op_sel_hi:[1,0]
	global_store_dwordx2 v[52:53], v[16:17], off offset:96
	v_pk_mul_f32 v[16:17], v[28:29], v[48:49] op_sel_hi:[1,0]
	v_pk_mul_f32 v[18:19], v[30:31], v[48:49] op_sel_hi:[1,0]
	v_cvt_pk_bf16_f32 v32, v32, v33
	v_cvt_pk_bf16_f32 v33, v34, v35
	v_cvt_pk_bf16_f32 v16, v16, v17
	v_cvt_pk_bf16_f32 v17, v18, v19
	s_mov_b64 s[14:15], 0
	global_store_dwordx2 v[52:53], v[32:33], off offset:48
	global_store_dwordx2 v[52:53], v[16:17], off offset:112

.LBB0_952:
	s_barrier
	s_and_saveexec_b64 s[14:15], s[0:1]
	s_cbranch_execz .LBB0_956
	s_cmp_eq_u32 s39, 0
	s_cbranch_scc1 .Lpop_cold
	v_mov_b32_e32 v16, s38
	v_mov_b32_e32 v17, s48
	ds_write_b32 v17, v16
	s_branch .LBB0_956
.Lpop_cold:
	s_mov_b64 s[18:19], exec
	v_mbcnt_lo_u32_b32 v16, s18, 0
	v_mbcnt_hi_u32_b32 v16, s19, v16
	v_cmp_eq_u32_e32 vcc, 0, v16
	s_and_saveexec_b64 s[16:17], vcc
	s_cbranch_execz .LBB0_955
	s_bcnt1_i32_b64 s18, s[18:19]
	v_mov_b32_e32 v17, s18
	global_atomic_add v17, v209, v17, s[10:11] offset:2048 sc0

.LBB0_956:
	s_or_b64 exec, exec, s[14:15]
	v_mov_b32_e32 v16, s48
	s_waitcnt lgkmcnt(0)
	s_barrier
	ds_read_b32 v16, v16
	s_mov_b64 s[14:15], -1
	s_waitcnt lgkmcnt(0)
	v_readfirstlane_b32 s24, v16
	s_cmpk_gt_i32 s24, 0x1ff
	s_cbranch_scc1 .LBB0_951
	s_mov_b32 s39, 1
	s_and_b32 s26, s24, 31
	s_mul_i32 s14, s26, 0xc0000
	s_add_u32 s16, s20, s14
	s_addc_u32 s17, s21, 0
	v_lshl_add_u64 v[16:17], s[16:17], 0, v[174:175]
	s_waitcnt vmcnt(8)
	v_lshl_add_u64 v[104:105], v[166:167], 1, v[16:17]
	global_load_dwordx4 v[92:95], v[104:105], off
	s_mov_b32 s15, s65
	s_and_saveexec_b64 s[18:19], s[2:3]
	s_cbranch_execz .LBB0_959
	v_lshl_add_u64 v[16:17], s[16:17], 0, v[176:177]
	v_lshl_add_u64 v[16:17], v[170:171], 1, v[16:17]
	global_load_dwordx4 v[80:83], v[16:17], off

.LBB0_980:
	s_waitcnt lgkmcnt(0)
	s_barrier
	s_waitcnt vmcnt(0)
	s_sub_i32 s16, s26, 4
	s_cmp_lg_u32 s30, s16
	s_cbranch_scc1 .Lpop_nopf
	s_and_saveexec_b64 s[16:17], s[0:1]
	s_cbranch_execz .Lpop_pf
	v_mov_b32_e32 v243, 1
	global_atomic_add v241, v209, v243, s[10:11] offset:2048 sc0

.Lpop_nopf:
	s_cmp_ge_u32 s30, s25
	s_cbranch_scc1 .LBB0_985
	v_lshl_add_u64 v[50:51], v[218:219], 0, s[34:35]
	global_load_dwordx4 v[84:87], v[50:51], off
	s_and_saveexec_b64 s[18:19], s[2:3]
	s_cbranch_execz .LBB0_983
	v_lshl_add_u64 v[50:51], v[216:217], 0, s[34:35]
	global_load_dwordx4 v[80:83], v[50:51], off
